# stack5 + pipelined out-proj epilogue x-loads + P6 and P1 modulation-table loops unrolled (all loads in flight, one wait)
# speedup vs baseline: 1.0143x; 1.0057x over previous
; __device__ __forceinline__ void p1_norm1(const Params& P, LAS unsigned char* lds, int tid, int blk, int G) {
;     ...
;         for (int k = tid; k < 2048; k += NTHREADS) {
;             const int js = 2048 + k, jh = k;
;             const float sc = bada[js] + ((modp[(size_t)(0 * 8 + b) * NMOD + js] + modp[(size_t)(1 * 8 + b) * NMOD + js]) + (modp[(size_t)(2 * 8 + b) * NMOD + js] + modp[(size_t)(3 * 8 + b) * NMOD + js]));
;             const float sv = bada[jh] + ((modp[(size_t)(0 * 8 + b) * NMOD + jh] + modp[(size_t)(1 * 8 + b) * NMOD + jh]) + (modp[(size_t)(2 * 8 + b) * NMOD + jh] + modp[(size_t)(3 * 8 + b) * NMOD + jh]));
;             gm[k] = P.in[4][k] * (1.0f + sc); sh[k] = sv;
;         }
.LBB0_167:
	v_lshl_add_u64 v[36:37], s[24:25], 0, v[74:75]
	v_add_co_u32_e32 v42, vcc, 0x2000, v36
	v_lshl_add_u64 v[38:39], s[8:9], 0, v[74:75]
	v_lshl_add_u64 v[40:41], s[14:15], 0, v[74:75]
	v_addc_co_u32_e32 v43, vcc, 0, v37, vcc
	global_load_dword v130, v[40:41], off
	v_add_co_u32_e32 v40, vcc, 0x308000, v38
	global_load_dword v131, v[42:43], off
	s_nop 0
	v_addc_co_u32_e32 v41, vcc, 0, v39, vcc
	v_add_co_u32_e32 v42, vcc, 0x368000, v38
	s_add_u32 s24, s24, 0x800
	s_nop 0
	v_addc_co_u32_e32 v43, vcc, 0, v39, vcc
	v_add_co_u32_e32 v44, vcc, 0x3c8000, v38
	global_load_dword v132, v[40:41], off
	global_load_dword v133, v[42:43], off
	v_addc_co_u32_e32 v45, vcc, 0, v39, vcc
	v_add_co_u32_e32 v40, vcc, 0x428000, v38
	s_addc_u32 s25, s25, 0
	s_nop 0
	v_addc_co_u32_e32 v41, vcc, 0, v39, vcc
	v_add_co_u32_e32 v42, vcc, 0x306000, v38
	global_load_dword v134, v[44:45], off
	global_load_dword v135, v[40:41], off
	v_addc_co_u32_e32 v43, vcc, 0, v39, vcc
	v_add_co_u32_e32 v40, vcc, 0x366000, v38
	s_add_u32 s8, s8, 0x800
	s_nop 0
	v_addc_co_u32_e32 v41, vcc, 0, v39, vcc
	v_add_co_u32_e32 v44, vcc, 0x3c6000, v38
	global_load_dword v136, v[42:43], off
	s_nop 0
	global_load_dword v137, v[40:41], off
	v_addc_co_u32_e32 v45, vcc, 0, v39, vcc
	v_add_co_u32_e32 v38, vcc, 0x426000, v38
	s_addc_u32 s9, s9, 0
	s_nop 0
	v_addc_co_u32_e32 v39, vcc, 0, v39, vcc
	global_load_dword v138, v[44:45], off
	s_nop 0
	global_load_dword v139, v[38:39], off
	s_nop 0
	global_load_dword v140, v[36:37], off
	s_add_u32 s14, s14, 0x800
	s_addc_u32 s15, s15, 0
	v_lshl_add_u64 v[36:37], s[24:25], 0, v[74:75]
	v_add_co_u32_e32 v42, vcc, 0x2000, v36
	v_lshl_add_u64 v[38:39], s[8:9], 0, v[74:75]
	v_lshl_add_u64 v[40:41], s[14:15], 0, v[74:75]
	v_addc_co_u32_e32 v43, vcc, 0, v37, vcc
	global_load_dword v142, v[40:41], off
	v_add_co_u32_e32 v40, vcc, 0x308000, v38
	global_load_dword v143, v[42:43], off
	s_nop 0
	v_addc_co_u32_e32 v41, vcc, 0, v39, vcc
	v_add_co_u32_e32 v42, vcc, 0x368000, v38
	s_add_u32 s24, s24, 0x800
	s_nop 0
	v_addc_co_u32_e32 v43, vcc, 0, v39, vcc
	v_add_co_u32_e32 v44, vcc, 0x3c8000, v38
	global_load_dword v144, v[40:41], off
	global_load_dword v145, v[42:43], off
	v_addc_co_u32_e32 v45, vcc, 0, v39, vcc
	v_add_co_u32_e32 v40, vcc, 0x428000, v38
	s_addc_u32 s25, s25, 0
	s_nop 0
	v_addc_co_u32_e32 v41, vcc, 0, v39, vcc
	v_add_co_u32_e32 v42, vcc, 0x306000, v38
	global_load_dword v146, v[44:45], off
	global_load_dword v147, v[40:41], off
	v_addc_co_u32_e32 v43, vcc, 0, v39, vcc
	v_add_co_u32_e32 v40, vcc, 0x366000, v38
	s_add_u32 s8, s8, 0x800
	s_nop 0
	v_addc_co_u32_e32 v41, vcc, 0, v39, vcc
	v_add_co_u32_e32 v44, vcc, 0x3c6000, v38
	global_load_dword v148, v[42:43], off
	s_nop 0
	global_load_dword v149, v[40:41], off
	v_addc_co_u32_e32 v45, vcc, 0, v39, vcc
	v_add_co_u32_e32 v38, vcc, 0x426000, v38
	s_addc_u32 s9, s9, 0
	s_nop 0
	v_addc_co_u32_e32 v39, vcc, 0, v39, vcc
	global_load_dword v150, v[44:45], off
	s_nop 0
	global_load_dword v151, v[38:39], off
	s_nop 0
	global_load_dword v152, v[36:37], off
	s_add_u32 s14, s14, 0x800
	s_addc_u32 s15, s15, 0
	v_lshl_add_u64 v[36:37], s[24:25], 0, v[74:75]
	v_add_co_u32_e32 v42, vcc, 0x2000, v36
	v_lshl_add_u64 v[38:39], s[8:9], 0, v[74:75]
	v_lshl_add_u64 v[40:41], s[14:15], 0, v[74:75]
	v_addc_co_u32_e32 v43, vcc, 0, v37, vcc
	global_load_dword v154, v[40:41], off
	v_add_co_u32_e32 v40, vcc, 0x308000, v38
	global_load_dword v155, v[42:43], off
	s_nop 0
	v_addc_co_u32_e32 v41, vcc, 0, v39, vcc
	v_add_co_u32_e32 v42, vcc, 0x368000, v38
	s_add_u32 s24, s24, 0x800
	s_nop 0
	v_addc_co_u32_e32 v43, vcc, 0, v39, vcc
	v_add_co_u32_e32 v44, vcc, 0x3c8000, v38
	global_load_dword v156, v[40:41], off
	global_load_dword v157, v[42:43], off
	v_addc_co_u32_e32 v45, vcc, 0, v39, vcc
	v_add_co_u32_e32 v40, vcc, 0x428000, v38
	s_addc_u32 s25, s25, 0
	s_nop 0
	v_addc_co_u32_e32 v41, vcc, 0, v39, vcc
	v_add_co_u32_e32 v42, vcc, 0x306000, v38
	global_load_dword v158, v[44:45], off
	global_load_dword v159, v[40:41], off
	v_addc_co_u32_e32 v43, vcc, 0, v39, vcc
	v_add_co_u32_e32 v40, vcc, 0x366000, v38
	s_add_u32 s8, s8, 0x800
	s_nop 0
	v_addc_co_u32_e32 v41, vcc, 0, v39, vcc
	v_add_co_u32_e32 v44, vcc, 0x3c6000, v38
	global_load_dword v160, v[42:43], off
	s_nop 0
	global_load_dword v161, v[40:41], off
	v_addc_co_u32_e32 v45, vcc, 0, v39, vcc
	v_add_co_u32_e32 v38, vcc, 0x426000, v38
	s_addc_u32 s9, s9, 0
	s_nop 0
	v_addc_co_u32_e32 v39, vcc, 0, v39, vcc
	global_load_dword v162, v[44:45], off
	s_nop 0
	global_load_dword v163, v[38:39], off
	s_nop 0
	global_load_dword v164, v[36:37], off
	s_add_u32 s14, s14, 0x800
	s_addc_u32 s15, s15, 0
	v_lshl_add_u64 v[36:37], s[24:25], 0, v[74:75]
	v_add_co_u32_e32 v42, vcc, 0x2000, v36
	v_lshl_add_u64 v[38:39], s[8:9], 0, v[74:75]
	v_lshl_add_u64 v[40:41], s[14:15], 0, v[74:75]
	v_addc_co_u32_e32 v43, vcc, 0, v37, vcc
	global_load_dword v166, v[40:41], off
	v_add_co_u32_e32 v40, vcc, 0x308000, v38
	global_load_dword v167, v[42:43], off
	s_nop 0
	v_addc_co_u32_e32 v41, vcc, 0, v39, vcc
	v_add_co_u32_e32 v42, vcc, 0x368000, v38
	s_add_u32 s24, s24, 0x800
	s_nop 0
	v_addc_co_u32_e32 v43, vcc, 0, v39, vcc
	v_add_co_u32_e32 v44, vcc, 0x3c8000, v38
	global_load_dword v168, v[40:41], off
	global_load_dword v169, v[42:43], off
	v_addc_co_u32_e32 v45, vcc, 0, v39, vcc
	v_add_co_u32_e32 v40, vcc, 0x428000, v38
	s_addc_u32 s25, s25, 0
	s_nop 0
	v_addc_co_u32_e32 v41, vcc, 0, v39, vcc
	v_add_co_u32_e32 v42, vcc, 0x306000, v38
	global_load_dword v170, v[44:45], off
	global_load_dword v171, v[40:41], off
	v_addc_co_u32_e32 v43, vcc, 0, v39, vcc
	v_add_co_u32_e32 v40, vcc, 0x366000, v38
	s_add_u32 s8, s8, 0x800
	s_nop 0
	v_addc_co_u32_e32 v41, vcc, 0, v39, vcc
	v_add_co_u32_e32 v44, vcc, 0x3c6000, v38
	global_load_dword v172, v[42:43], off
	s_nop 0
	global_load_dword v173, v[40:41], off
	v_addc_co_u32_e32 v45, vcc, 0, v39, vcc
	v_add_co_u32_e32 v38, vcc, 0x426000, v38
	s_addc_u32 s9, s9, 0
	s_nop 0
	v_addc_co_u32_e32 v39, vcc, 0, v39, vcc
	global_load_dword v174, v[44:45], off
	s_nop 0
	global_load_dword v175, v[38:39], off
	s_nop 0
	global_load_dword v176, v[36:37], off
	s_add_u32 s14, s14, 0x800
	s_addc_u32 s15, s15, 0
	s_waitcnt vmcnt(0)
; __device__ __forceinline__ void p1_norm1(const Params& P, LAS unsigned char* lds, int tid, int blk, int G) {
;     ...
;         for (int k = tid; k < 2048; k += NTHREADS) {
;             const int js = 2048 + k, jh = k;
;             const float sc = bada[js] + ((modp[(size_t)(0 * 8 + b) * NMOD + js] + modp[(size_t)(1 * 8 + b) * NMOD + js]) + (modp[(size_t)(2 * 8 + b) * NMOD + js] + modp[(size_t)(3 * 8 + b) * NMOD + js]));
;             const float sv = bada[jh] + ((modp[(size_t)(0 * 8 + b) * NMOD + jh] + modp[(size_t)(1 * 8 + b) * NMOD + jh]) + (modp[(size_t)(2 * 8 + b) * NMOD + jh] + modp[(size_t)(3 * 8 + b) * NMOD + jh]));
;             gm[k] = P.in[4][k] * (1.0f + sc); sh[k] = sv;
;         }
;         __syncthreads();
;         if (rb != blk) { const float* xr = P.in[0] + (size_t)(rb * 64 + wave * 8) * DM;
; #pragma unroll
;           for (int i = 0; i < 8; ++i) v[i] = *(const f32x4*)(xr + (i * 64 + lane) * 4); }
	v_add_f32_e32 v37, v132, v133
	v_add_f32_e32 v39, v134, v135
	v_add_f32_e32 v37, v37, v39
	v_add_f32_e32 v37, v131, v37
	v_add_f32_e32 v37, 1.0, v37
	v_mul_f32_e32 v37, v37, v130
	v_add_f32_e32 v39, v136, v137
	v_add_f32_e32 v38, v138, v139
	v_add_f32_e32 v38, v39, v38
	v_add_f32_e32 v36, v140, v38
	ds_write2st64_b32 v34, v37, v36 offset1:32
	v_add_u32_e32 v34, 0x800, v34
	v_add_f32_e32 v37, v144, v145
	v_add_f32_e32 v39, v146, v147
	v_add_f32_e32 v37, v37, v39
	v_add_f32_e32 v37, v143, v37
	v_add_f32_e32 v37, 1.0, v37
	v_mul_f32_e32 v37, v37, v142
	v_add_f32_e32 v39, v148, v149
	v_add_f32_e32 v38, v150, v151
	v_add_f32_e32 v38, v39, v38
	v_add_f32_e32 v36, v152, v38
	ds_write2st64_b32 v34, v37, v36 offset1:32
	v_add_u32_e32 v34, 0x800, v34
	v_add_f32_e32 v37, v156, v157
	v_add_f32_e32 v39, v158, v159
	v_add_f32_e32 v37, v37, v39
	v_add_f32_e32 v37, v155, v37
	v_add_f32_e32 v37, 1.0, v37
	v_mul_f32_e32 v37, v37, v154
	v_add_f32_e32 v39, v160, v161
	v_add_f32_e32 v38, v162, v163
	v_add_f32_e32 v38, v39, v38
	v_add_f32_e32 v36, v164, v38
	ds_write2st64_b32 v34, v37, v36 offset1:32
	v_add_u32_e32 v34, 0x800, v34
	v_add_f32_e32 v37, v168, v169
	v_add_f32_e32 v39, v170, v171
	v_add_f32_e32 v37, v37, v39
	v_add_f32_e32 v37, v167, v37
	v_add_f32_e32 v37, 1.0, v37
	v_mul_f32_e32 v37, v37, v166
	v_add_f32_e32 v39, v172, v173
	v_add_f32_e32 v38, v174, v175
	v_add_f32_e32 v38, v39, v38
	v_add_f32_e32 v36, v176, v38
	ds_write2st64_b32 v34, v37, v36 offset1:32
	s_or_b64 exec, exec, s[10:11]
	s_cmp_lg_u32 s34, s2
	s_mov_b64 s[8:9], -1
	s_waitcnt lgkmcnt(0)
	s_barrier
	s_cbranch_scc0 .LBB0_170
	v_lshl_or_b32 v86, s34, 6, v1
	v_ashrrev_i32_e32 v87, 31, v86
	v_lshlrev_b64 v[66:67], 13, v[86:87]
	v_lshl_add_u64 v[50:51], v[76:77], 0, v[66:67]
	v_add_co_u32_e32 v62, vcc, 0x1000, v50
	global_load_dwordx4 v[34:37], v[50:51], off
	global_load_dwordx4 v[38:41], v[50:51], off offset:1024
	global_load_dwordx4 v[42:45], v[50:51], off offset:2048
	global_load_dwordx4 v[46:49], v[50:51], off offset:3072
	v_addc_co_u32_e32 v63, vcc, 0, v51, vcc
	global_load_dwordx4 v[50:53], v[62:63], off
	global_load_dwordx4 v[54:57], v[62:63], off offset:1024
	global_load_dwordx4 v[58:61], v[62:63], off offset:2048
	s_nop 0
	global_load_dwordx4 v[62:65], v[62:63], off offset:3072
	s_mov_b64 s[8:9], 0
	v_mov_b64_e32 v[68:69], v[86:87]

; #define G8_STAGE(bufoff, gbase, v0, v1) do { unsigned x0_ = (v0), x1_ = (v1); asm volatile("" : "+v"(x0_), "+v"(x1_));     \
;         __builtin_amdgcn_global_load_lds((const unsigned*)((gbase) + x0_), (LAS unsigned*)(lds + (bufoff) + ldsw), 16, 0, 0); \
;         __builtin_amdgcn_global_load_lds((const unsigned*)((gbase) + x1_), (LAS unsigned*)(lds + (bufoff) + ldsw + 8192), 16, 0, 0); } while (0)
; #define G8_LDA(dst, b, h) do { _Pragma("unroll") for (int m = 0; m < 4; ++m) _Pragma("unroll") for (int k = 0; k < 2; ++k) dst[m][k] = *(const LAS bf16x8*)(lds + G8_SA(b, h) + aoff + m * 2048 + k * 1024); } while (0)
; #define G8_LDB(dst, b, h) do { _Pragma("unroll") for (int n = 0; n < 2; ++n) _Pragma("unroll") for (int k = 0; k < 2; ++k) dst[n][k] = *(const LAS bf16x8*)(lds + G8_SB(b, h) + boff + n * 2048 + k * 1024); } while (0)
; #define G8_WAIT_V(n) asm volatile("s_waitcnt vmcnt(" #n ")" ::: "memory")
; #define G8_WAIT_L(n) asm volatile("s_waitcnt lgkmcnt(" #n ")" ::: "memory")
; #define G8_BAR __builtin_amdgcn_s_barrier()
; #define G8_SCHED __builtin_amdgcn_sched_barrier(0)
;     ...
;             G8_CONV_READ; G8_SCHED;
;             G8_LDB(B0, 0, 0); G8_SCHED; G8_LDA(At, 0, 0); G8_STAGE(G8_SA(1, 1), a1, cv[1][0], cv[1][1]);
;             G8_WAIT_L(8); G8_BAR; G8_WAIT_L(0); if (do0) G8_MMA(0, 0, At, B0); G8_CONV_CVT; G8_BAR; G8_SCHED;
;             G8_LDB(B1, 0, 1); G8_STAGE(G8_SB(0, 0), b2, voffB[0], voffB[1]);
;             G8_BAR; G8_CONV_ISSUE;
;             G8_WAIT_L(0); if (do0) G8_MMA(0, 1, At, B1); G8_BAR;
;             G8_LDA(At, 0, 1); G8_STAGE(G8_SA(0, 0), a2, o00, o01);
;             G8_BAR; G8_WAIT_L(0); if (do1) G8_MMA(1, 0, At, B0); G8_BAR; G8_SCHED;
;             G8_STAGE(G8_SB(0, 1), b2 + hstepB, voffB[0], voffB[1]);
;             if constexpr (CONV) G8_WAIT_V(9); else G8_WAIT_V(6);
;             G8_BAR; if (do1) G8_MMA(1, 1, At, B1); G8_BAR;
.LBB0_741:
	s_add_u32 s70, s0, 0x80
	s_addc_u32 s71, s1, 0
	s_add_u32 s0, s0, 0x100
	s_addc_u32 s1, s1, 0
	s_add_u32 s34, s34, 0x10000
	s_addc_u32 s35, s35, 0
	s_cmp_eq_u32 s68, 4
	s_cselect_b32 s39, s64, s1
	s_cselect_b32 s38, s65, s0
	s_cselect_b32 s37, s66, s35
	s_cselect_b32 s36, s67, s34
	v_add_u32_e32 v2, s51, v183
	ds_read_b128 v[134:137], v2
	ds_read_b128 v[138:141], v2 offset:1024
	ds_read_b128 v[142:145], v2 offset:2048
	ds_read_b128 v[146:149], v2 offset:3072
	v_mov_b32_e32 v2, v182
	v_mov_b32_e32 v4, v181
	s_add_i32 m0, s41, 0xc000
	ds_read_b128 v[154:157], v184
	ds_read_b128 v[158:161], v184 offset:1024
	ds_read_b128 v[162:165], v184 offset:2048
	ds_read_b128 v[166:169], v184 offset:3072
	ds_read_b128 v[170:173], v184 offset:4096
	ds_read_b128 v[174:177], v184 offset:5120
	ds_read_b128 v[188:191], v184 offset:6144
	ds_read_b128 v[192:195], v184 offset:7168
	s_nop 0
	global_load_lds_dwordx4 v4, s[70:71]
	s_add_i32 m0, s41, 0xe000
	s_nop 0
	global_load_lds_dwordx4 v2, s[70:71]
	s_waitcnt lgkmcnt(8)
	s_barrier
	s_waitcnt lgkmcnt(0)
	s_setprio 1
	s_waitcnt lgkmcnt(0)
	v_mfma_scale_f32_16x16x128_f8f6f4 v[196:199], v[134:141], v[154:161], v[6:9], v185, v185 op_sel_hi:[0,0,0]
	v_mfma_scale_f32_16x16x128_f8f6f4 v[200:203], v[142:149], v[154:161], v[10:13], v185, v185 op_sel_hi:[0,0,0]
	v_mfma_scale_f32_16x16x128_f8f6f4 v[204:207], v[134:141], v[162:169], v[14:17], v185, v185 op_sel_hi:[0,0,0]
	v_mfma_scale_f32_16x16x128_f8f6f4 v[208:211], v[142:149], v[162:169], v[18:21], v185, v185 op_sel_hi:[0,0,0]
	v_mfma_scale_f32_16x16x128_f8f6f4 v[212:215], v[134:141], v[170:177], v[22:25], v185, v185 op_sel_hi:[0,0,0]
	v_mfma_scale_f32_16x16x128_f8f6f4 v[216:219], v[142:149], v[170:177], v[26:29], v185, v185 op_sel_hi:[0,0,0]
	v_mfma_scale_f32_16x16x128_f8f6f4 v[220:223], v[134:141], v[188:195], v[30:33], v185, v185 op_sel_hi:[0,0,0]
	v_mfma_scale_f32_16x16x128_f8f6f4 v[224:227], v[142:149], v[188:195], v[34:37], v185, v185 op_sel_hi:[0,0,0]
	s_setprio 0
	s_barrier
	v_add_u32_e32 v2, s52, v183
	s_add_i32 s69, s51, s40
	ds_read_b128 v[4:7], v2
	ds_read_b128 v[8:11], v2 offset:1024
	ds_read_b128 v[12:15], v2 offset:2048
	ds_read_b128 v[16:19], v2 offset:3072
	v_mov_b32_e32 v2, v178
	v_mov_b32_e32 v20, v1
	s_mov_b32 m0, s69
	s_nop 0
	global_load_lds_dwordx4 v20, s[36:37]
	s_add_i32 m0, s69, 0x2000
	s_nop 0
	global_load_lds_dwordx4 v2, s[36:37]
	s_barrier
	s_waitcnt lgkmcnt(0)
	s_setprio 1
	s_waitcnt lgkmcnt(0)
	v_mfma_scale_f32_16x16x128_f8f6f4 v[228:231], v[4:11], v[154:161], v[38:41], v185, v185 op_sel_hi:[0,0,0]
	v_mfma_scale_f32_16x16x128_f8f6f4 v[232:235], v[12:19], v[154:161], v[42:45], v185, v185 op_sel_hi:[0,0,0]
	v_mfma_scale_f32_16x16x128_f8f6f4 v[236:239], v[4:11], v[162:169], v[46:49], v185, v185 op_sel_hi:[0,0,0]
	v_mfma_scale_f32_16x16x128_f8f6f4 v[240:243], v[12:19], v[162:169], v[50:53], v185, v185 op_sel_hi:[0,0,0]
	v_mfma_scale_f32_16x16x128_f8f6f4 v[244:247], v[4:11], v[170:177], v[54:57], v185, v185 op_sel_hi:[0,0,0]
	v_mfma_scale_f32_16x16x128_f8f6f4 v[170:173], v[12:19], v[170:177], v[58:61], v185, v185 op_sel_hi:[0,0,0]
	v_mfma_scale_f32_16x16x128_f8f6f4 v[174:177], v[4:11], v[188:195], v[62:65], v185, v185 op_sel_hi:[0,0,0]
	v_mfma_scale_f32_16x16x128_f8f6f4 v[188:191], v[12:19], v[188:195], v[66:69], v185, v185 op_sel_hi:[0,0,0]
	s_setprio 0
	v_mov_b32_e32 v2, v179
	s_nop 0
	v_mov_b32_e32 v52, v180
	s_mov_b32 m0, s41
	s_barrier
	ds_read_b128 v[20:23], v184 offset:16384
	ds_read_b128 v[24:27], v184 offset:17408
	ds_read_b128 v[28:31], v184 offset:18432
	ds_read_b128 v[32:35], v184 offset:19456
	ds_read_b128 v[36:39], v184 offset:20480
	ds_read_b128 v[40:43], v184 offset:21504
	ds_read_b128 v[44:47], v184 offset:22528
	ds_read_b128 v[48:51], v184 offset:23552
	s_nop 0
	global_load_lds_dwordx4 v2, s[38:39]
	s_mov_b32 m0, s42
	s_nop 0
	global_load_lds_dwordx4 v52, s[38:39]
	s_barrier
	s_waitcnt lgkmcnt(0)
	s_setprio 1
	s_waitcnt lgkmcnt(0)
	v_mfma_scale_f32_16x16x128_f8f6f4 v[74:77], v[142:149], v[20:27], v[74:77], v185, v185 op_sel_hi:[0,0,0]
	v_mfma_scale_f32_16x16x128_f8f6f4 v[78:81], v[134:141], v[28:35], v[78:81], v185, v185 op_sel_hi:[0,0,0]
	v_mfma_scale_f32_16x16x128_f8f6f4 v[82:85], v[142:149], v[28:35], v[82:85], v185, v185 op_sel_hi:[0,0,0]
	v_mfma_scale_f32_16x16x128_f8f6f4 v[86:89], v[134:141], v[36:43], v[86:89], v185, v185 op_sel_hi:[0,0,0]
	v_mfma_scale_f32_16x16x128_f8f6f4 v[90:93], v[142:149], v[36:43], v[90:93], v185, v185 op_sel_hi:[0,0,0]
	v_mfma_scale_f32_16x16x128_f8f6f4 v[94:97], v[134:141], v[44:51], v[94:97], v185, v185 op_sel_hi:[0,0,0]
	v_mfma_scale_f32_16x16x128_f8f6f4 v[98:101], v[142:149], v[44:51], v[98:101], v185, v185 op_sel_hi:[0,0,0]
	v_mfma_scale_f32_16x16x128_f8f6f4 v[248:251], v[134:141], v[20:27], v[70:73], v185, v185 op_sel_hi:[0,0,0]
	s_setprio 0
	s_barrier
	s_add_u32 s70, s36, 0x4000
	s_addc_u32 s71, s37, 0
	s_add_i32 s69, s52, s40
	v_mov_b32_e32 v2, v178
	v_mov_b32_e32 v52, v1
	s_mov_b32 m0, s69
	s_nop 0
	global_load_lds_dwordx4 v52, s[70:71]
	s_add_i32 m0, s69, 0x2000
	s_nop 0
	global_load_lds_dwordx4 v2, s[70:71]
	s_waitcnt vmcnt(6)
	s_barrier
	s_setprio 1
	v_mfma_scale_f32_16x16x128_f8f6f4 v[102:105], v[4:11], v[20:27], v[102:105], v185, v185 op_sel_hi:[0,0,0]
	v_mfma_scale_f32_16x16x128_f8f6f4 v[106:109], v[12:19], v[20:27], v[106:109], v185, v185 op_sel_hi:[0,0,0]
	v_mfma_scale_f32_16x16x128_f8f6f4 v[110:113], v[4:11], v[28:35], v[110:113], v185, v185 op_sel_hi:[0,0,0]
	v_mfma_scale_f32_16x16x128_f8f6f4 v[114:117], v[12:19], v[28:35], v[114:117], v185, v185 op_sel_hi:[0,0,0]
	v_mfma_scale_f32_16x16x128_f8f6f4 v[118:121], v[4:11], v[36:43], v[118:121], v185, v185 op_sel_hi:[0,0,0]
	v_mfma_scale_f32_16x16x128_f8f6f4 v[122:125], v[12:19], v[36:43], v[122:125], v185, v185 op_sel_hi:[0,0,0]
	v_mfma_scale_f32_16x16x128_f8f6f4 v[126:129], v[4:11], v[44:51], v[126:129], v185, v185 op_sel_hi:[0,0,0]
	v_mfma_scale_f32_16x16x128_f8f6f4 v[130:133], v[12:19], v[44:51], v[130:133], v185, v185 op_sel_hi:[0,0,0]
	s_setprio 0
	s_add_i32 s69, 0, 0x18000
	v_add_u32_e32 v2, s69, v183
	s_barrier
; #define G8_STAGE(bufoff, gbase, v0, v1) do { unsigned x0_ = (v0), x1_ = (v1); asm volatile("" : "+v"(x0_), "+v"(x1_));     \
;         __builtin_amdgcn_global_load_lds((const unsigned*)((gbase) + x0_), (LAS unsigned*)(lds + (bufoff) + ldsw), 16, 0, 0); \
;         __builtin_amdgcn_global_load_lds((const unsigned*)((gbase) + x1_), (LAS unsigned*)(lds + (bufoff) + ldsw + 8192), 16, 0, 0); } while (0)
; #define G8_LDA(dst, b, h) do { _Pragma("unroll") for (int m = 0; m < 4; ++m) _Pragma("unroll") for (int k = 0; k < 2; ++k) dst[m][k] = *(const LAS bf16x8*)(lds + G8_SA(b, h) + aoff + m * 2048 + k * 1024); } while (0)
; #define G8_LDB(dst, b, h) do { _Pragma("unroll") for (int n = 0; n < 2; ++n) _Pragma("unroll") for (int k = 0; k < 2; ++k) dst[n][k] = *(const LAS bf16x8*)(lds + G8_SB(b, h) + boff + n * 2048 + k * 1024); } while (0)
; #define G8_WAIT_V(n) asm volatile("s_waitcnt vmcnt(" #n ")" ::: "memory")
; #define G8_WAIT_L(n) asm volatile("s_waitcnt lgkmcnt(" #n ")" ::: "memory")
; #define G8_BAR __builtin_amdgcn_s_barrier()
; #define G8_SCHED __builtin_amdgcn_sched_barrier(0)
;     ...
;             G8_LDB(B0, 1, 0); G8_SCHED; G8_LDA(At, 1, 0); G8_STAGE(G8_SA(0, 1), a2, o10, o11);
;             G8_WAIT_L(8); G8_BAR; G8_WAIT_L(0); if (do0) G8_MMA(0, 0, At, B0); G8_BAR; G8_SCHED;
;             G8_LDB(B1, 1, 1); G8_STAGE(G8_SB(1, 0), b3, voffB[0], voffB[1]);
;             G8_BAR; G8_WAIT_L(0); if (do0) G8_MMA(0, 1, At, B1); G8_BAR;
;             G8_LDA(At, 1, 1); G8_STAGE(G8_SA(1, 0), a3, o00, o01);
;             G8_BAR; G8_WAIT_L(0); if (do1) G8_MMA(1, 0, At, B0); G8_BAR; G8_SCHED;
;             G8_STAGE(G8_SB(1, 1), b3 + hstepB, voffB[0], voffB[1]);
;             G8_WAIT_V(6); G8_BAR; if (do1) G8_MMA(1, 1, At, B1); G8_BAR;
	ds_read_b128 v[134:137], v2
	ds_read_b128 v[138:141], v2 offset:1024
	ds_read_b128 v[142:145], v2 offset:2048
	ds_read_b128 v[146:149], v2 offset:3072
	v_mov_b32_e32 v2, v182
	v_mov_b32_e32 v4, v181
	s_mov_b32 m0, s43
	ds_read_b128 v[42:45], v184 offset:32768
	ds_read_b128 v[46:49], v184 offset:33792
	ds_read_b128 v[50:53], v184 offset:34816
	ds_read_b128 v[54:57], v184 offset:35840
	ds_read_b128 v[58:61], v184 offset:36864
	ds_read_b128 v[62:65], v184 offset:37888
	ds_read_b128 v[66:69], v184 offset:38912
	ds_read_b128 v[70:73], v184 offset:39936
	s_nop 0
	global_load_lds_dwordx4 v4, s[38:39]
	s_mov_b32 m0, s44
	s_nop 0
	global_load_lds_dwordx4 v2, s[38:39]
	s_waitcnt lgkmcnt(8)
	s_barrier
	s_waitcnt lgkmcnt(0)
	s_setprio 1
	s_waitcnt lgkmcnt(0)
	v_mfma_scale_f32_16x16x128_f8f6f4 v[6:9], v[134:141], v[42:49], v[196:199], v185, v185 op_sel_hi:[0,0,0]
	v_mfma_scale_f32_16x16x128_f8f6f4 v[10:13], v[142:149], v[42:49], v[200:203], v185, v185 op_sel_hi:[0,0,0]
	v_mfma_scale_f32_16x16x128_f8f6f4 v[14:17], v[134:141], v[50:57], v[204:207], v185, v185 op_sel_hi:[0,0,0]
	v_mfma_scale_f32_16x16x128_f8f6f4 v[18:21], v[142:149], v[50:57], v[208:211], v185, v185 op_sel_hi:[0,0,0]
	v_mfma_scale_f32_16x16x128_f8f6f4 v[22:25], v[134:141], v[58:65], v[212:215], v185, v185 op_sel_hi:[0,0,0]
	v_mfma_scale_f32_16x16x128_f8f6f4 v[26:29], v[142:149], v[58:65], v[216:219], v185, v185 op_sel_hi:[0,0,0]
	v_mfma_scale_f32_16x16x128_f8f6f4 v[30:33], v[134:141], v[66:73], v[220:223], v185, v185 op_sel_hi:[0,0,0]
	v_mfma_scale_f32_16x16x128_f8f6f4 v[34:37], v[142:149], v[66:73], v[224:227], v185, v185 op_sel_hi:[0,0,0]
	s_setprio 0
	s_barrier
	s_add_i32 s72, 0, 0x1c000
	s_add_u32 s70, s36, 0x8000
	v_add_u32_e32 v2, s72, v183
	s_addc_u32 s71, s37, 0
	s_add_i32 s69, s69, s40
	ds_read_b128 v[154:157], v2
	ds_read_b128 v[158:161], v2 offset:1024
	ds_read_b128 v[162:165], v2 offset:2048
	ds_read_b128 v[166:169], v2 offset:3072
	v_mov_b32_e32 v2, v1
	v_mov_b32_e32 v4, v178
	s_mov_b32 m0, s69
	s_nop 0
	global_load_lds_dwordx4 v2, s[70:71]
	s_add_i32 m0, s69, 0x2000
	s_nop 0
	global_load_lds_dwordx4 v4, s[70:71]
	s_barrier
	s_waitcnt lgkmcnt(0)
	s_setprio 1
	s_waitcnt lgkmcnt(0)
	v_mfma_scale_f32_16x16x128_f8f6f4 v[38:41], v[154:161], v[42:49], v[228:231], v185, v185 op_sel_hi:[0,0,0]
	v_mfma_scale_f32_16x16x128_f8f6f4 v[42:45], v[162:169], v[42:49], v[232:235], v185, v185 op_sel_hi:[0,0,0]
	v_mfma_scale_f32_16x16x128_f8f6f4 v[46:49], v[154:161], v[50:57], v[236:239], v185, v185 op_sel_hi:[0,0,0]
	v_mfma_scale_f32_16x16x128_f8f6f4 v[50:53], v[162:169], v[50:57], v[240:243], v185, v185 op_sel_hi:[0,0,0]
	v_mfma_scale_f32_16x16x128_f8f6f4 v[54:57], v[154:161], v[58:65], v[244:247], v185, v185 op_sel_hi:[0,0,0]
	v_mfma_scale_f32_16x16x128_f8f6f4 v[58:61], v[162:169], v[58:65], v[170:173], v185, v185 op_sel_hi:[0,0,0]
	v_mfma_scale_f32_16x16x128_f8f6f4 v[62:65], v[154:161], v[66:73], v[174:177], v185, v185 op_sel_hi:[0,0,0]
	v_mfma_scale_f32_16x16x128_f8f6f4 v[66:69], v[162:169], v[66:73], v[188:191], v185, v185 op_sel_hi:[0,0,0]
	s_setprio 0
	v_mov_b32_e32 v4, v180
	v_mov_b32_e32 v2, v179
	s_barrier
	s_nop 0
	ds_read_b128 v[170:173], v184 offset:49152
	ds_read_b128 v[174:177], v184 offset:50176
	ds_read_b128 v[188:191], v184 offset:51200
	ds_read_b128 v[192:195], v184 offset:52224
	ds_read_b128 v[196:199], v184 offset:53248
	ds_read_b128 v[200:203], v184 offset:54272
	ds_read_b128 v[204:207], v184 offset:55296
	ds_read_b128 v[208:211], v184 offset:56320
	v_mov_b32_e32 v5, v3
	v_lshl_add_u64 v[70:71], s[38:39], 0, v[2:3]
	s_mov_b32 m0, s48
	v_lshl_add_u64 v[70:71], v[70:71], 0, s[14:15]
	v_lshl_add_u64 v[4:5], s[38:39], 0, v[4:5]
	global_load_lds_dwordx4 v[70:71], off
	v_lshl_add_u64 v[4:5], v[4:5], 0, s[14:15]
	s_mov_b32 m0, s49
	s_nop 0
	global_load_lds_dwordx4 v[4:5], off
	s_barrier
	s_waitcnt lgkmcnt(0)
	s_setprio 1
	s_waitcnt lgkmcnt(0)
	v_mfma_scale_f32_16x16x128_f8f6f4 v[70:73], v[134:141], v[170:177], v[248:251], v185, v185 op_sel_hi:[0,0,0]
	v_mfma_scale_f32_16x16x128_f8f6f4 v[74:77], v[142:149], v[170:177], v[74:77], v185, v185 op_sel_hi:[0,0,0]
	v_mfma_scale_f32_16x16x128_f8f6f4 v[78:81], v[134:141], v[188:195], v[78:81], v185, v185 op_sel_hi:[0,0,0]
	v_mfma_scale_f32_16x16x128_f8f6f4 v[82:85], v[142:149], v[188:195], v[82:85], v185, v185 op_sel_hi:[0,0,0]
	v_mfma_scale_f32_16x16x128_f8f6f4 v[86:89], v[134:141], v[196:203], v[86:89], v185, v185 op_sel_hi:[0,0,0]
	v_mfma_scale_f32_16x16x128_f8f6f4 v[90:93], v[142:149], v[196:203], v[90:93], v185, v185 op_sel_hi:[0,0,0]
	v_mfma_scale_f32_16x16x128_f8f6f4 v[94:97], v[134:141], v[204:211], v[94:97], v185, v185 op_sel_hi:[0,0,0]
	v_mfma_scale_f32_16x16x128_f8f6f4 v[98:101], v[142:149], v[204:211], v[98:101], v185, v185 op_sel_hi:[0,0,0]
	s_setprio 0
	s_barrier
	s_add_u32 s36, s36, 0xc000
	s_addc_u32 s37, s37, 0
	s_add_i32 s38, s72, s40
	v_mov_b32_e32 v2, v178
	v_mov_b32_e32 v4, v1
	s_mov_b32 m0, s38
	s_nop 0
	global_load_lds_dwordx4 v4, s[36:37]
	s_add_i32 m0, s38, 0x2000
	s_nop 0
	global_load_lds_dwordx4 v2, s[36:37]
	s_waitcnt vmcnt(6)
	s_barrier
	s_setprio 1
	v_mfma_scale_f32_16x16x128_f8f6f4 v[102:105], v[154:161], v[170:177], v[102:105], v185, v185 op_sel_hi:[0,0,0]
	v_mfma_scale_f32_16x16x128_f8f6f4 v[106:109], v[162:169], v[170:177], v[106:109], v185, v185 op_sel_hi:[0,0,0]
	v_mfma_scale_f32_16x16x128_f8f6f4 v[110:113], v[154:161], v[188:195], v[110:113], v185, v185 op_sel_hi:[0,0,0]
	v_mfma_scale_f32_16x16x128_f8f6f4 v[114:117], v[162:169], v[188:195], v[114:117], v185, v185 op_sel_hi:[0,0,0]
	v_mfma_scale_f32_16x16x128_f8f6f4 v[118:121], v[154:161], v[196:203], v[118:121], v185, v185 op_sel_hi:[0,0,0]
	v_mfma_scale_f32_16x16x128_f8f6f4 v[122:125], v[162:169], v[196:203], v[122:125], v185, v185 op_sel_hi:[0,0,0]
	v_mfma_scale_f32_16x16x128_f8f6f4 v[126:129], v[154:161], v[204:211], v[126:129], v185, v185 op_sel_hi:[0,0,0]
	v_mfma_scale_f32_16x16x128_f8f6f4 v[130:133], v[162:169], v[204:211], v[130:133], v185, v185 op_sel_hi:[0,0,0]
	s_setprio 0
	s_add_i32 s68, s68, 2
	s_cmp_gt_u32 s68, 5
	s_barrier
; __device__ __forceinline__ unsigned cvt_pk_bf16(float lo, float hi) { const f32x2 v = {lo, hi}; return __builtin_bit_cast(unsigned, __builtin_convertvector(v, bf16x2_t)); }
;     __device__ __forceinline__ void operator()(g8::Acc& acc, const g8::Unit& u, int wr, int wc, int fr, int fq) const {
;     ...
;         const int col0 = u.pn * 256 + wc * 32 + 8 * fq;
;         const int b = (u.pm * 256) >> 11;
;         f32x4 gt[2][2];
; #pragma unroll
;         for (int bj = 0; bj < 2; ++bj)
; #pragma unroll
;             for (int n = 0; n < 2; ++n) gt[bj][n] = *(const f32x4*)(mod + (size_t)b * NMOD + 2 * DM + col0 + bj * 128 + n * 4) * (1.0f / (CAT_SCALE * WOUT_SCALE));
; #pragma unroll
;         for (int am = 0; am < 4; ++am) {
;             const int ai = am >> 1, m0 = (am & 1) * 2;
;             f32x4 xv[2][2][2];
; #pragma unroll
;             for (int mm = 0; mm < 2; ++mm)
; #pragma unroll
;                 for (int bj = 0; bj < 2; ++bj) { const size_t off = (size_t)(row0 + ai * 128 + (m0 + mm) * 16) * DM + col0 + bj * 128; xv[mm][bj][0] = *(const f32x4*)(x + off); xv[mm][bj][1] = *(const f32x4*)(x + off + 4); }
; #pragma unroll
;             for (int mm = 0; mm < 2; ++mm) { const int m = m0 + mm; const int row = row0 + ai * 128 + m * 16; float ss = 0.f;
; #pragma unroll
;                 for (int bj = 0; bj < 2; ++bj) { const size_t off = (size_t)row * DM + col0 + bj * 128;
;                     const f32x4 o0 = xv[mm][bj][0] + gt[bj][0] * acc[ai][bj][m][0], o1 = xv[mm][bj][1] + gt[bj][1] * acc[ai][bj][m][1];
;                     ss += (o0[0] * o0[0] + o0[1] * o0[1]) + (o0[2] * o0[2] + o0[3] * o0[3]) + (o1[0] * o1[0] + o1[1] * o1[1]) + (o1[2] * o1[2] + o1[3] * o1[3]);
;                     u32x4 w; w.x = cvt_pk_bf16(o0[0], o0[1]); w.y = cvt_pk_bf16(o0[2], o0[3]); w.z = cvt_pk_bf16(o1[0], o1[1]); w.w = cvt_pk_bf16(o1[2], o1[3]);
;                     *(u32x4*)(X1 + off) = w; }
;                 ss += __shfl_xor(ss, 16); ss += __shfl_xor(ss, 32);
;                 if (fq == 0) rowss2[(size_t)row * 32 + u.pn * 4 + wc] = ss; }
	s_cbranch_scc0 .LBB0_741
	s_mov_b32 s0, 0
	s_cmp_lg_u32 s4, 0
	v_mbcnt_lo_u32_b32 v2, -1, s0
	v_mbcnt_hi_u32_b32 v154, -1, v2
	v_and_b32_e32 v2, 15, v154
	s_cbranch_scc0 .LBB0_764
	s_lshl_b32 s0, s63, 8
	s_add_i32 s0, s0, s46
	v_or_b32_e32 v170, s0, v2
	s_lshl_b32 s0, s62, 8
	v_lshrrev_b32_e32 v4, 1, v154
	v_and_b32_e32 v4, 0x7ffffff8, v4
	s_or_b32 s0, s0, s47
	v_add_u32_e32 v4, s0, v4
	s_ashr_i32 s0, s63, 3
	s_mul_hi_i32 s1, s0, 0xc000
	s_mul_i32 s0, s0, 0xc000
	v_readlane_b32 s36, v254, 39
	v_readlane_b32 s37, v254, 40
	s_add_u32 s0, s36, s0
	v_ashrrev_i32_e32 v5, 31, v4
	s_addc_u32 s1, s37, s1
	v_lshlrev_b64 v[134:135], 2, v[4:5]
	v_lshl_add_u64 v[136:137], s[0:1], 0, v[134:135]
	v_lshl_add_u64 v[138:139], v[136:137], 0, s[24:25]
	v_add_co_u32_e32 v136, vcc, s53, v136
	v_readlane_b32 s64, v254, 7
	s_nop 0
	v_addc_co_u32_e32 v137, vcc, 0, v137, vcc
	v_readlane_b32 s65, v254, 8
	v_ashrrev_i32_e32 v171, 31, v170
	global_load_dwordx4 v[156:159], v[136:137], off
	global_load_dwordx4 v[190:193], v[138:139], off offset:528
	global_load_dwordx4 v[160:163], v[138:139], off offset:16
	global_load_dwordx4 v[194:197], v[138:139], off offset:512
	v_lshl_add_u64 v[172:173], s[64:65], 0, v[134:135]
	v_lshlrev_b64 v[134:135], 13, v[170:171]
	v_lshl_add_u64 v[134:135], v[172:173], 0, v[134:135]
	global_load_dwordx4 v[198:201], v[134:135], off
	global_load_dwordx4 v[202:205], v[134:135], off offset:16
	global_load_dwordx4 v[206:209], v[134:135], off offset:512
	global_load_dwordx4 v[210:213], v[134:135], off offset:528
	v_or_b32_e32 v174, 16, v170
	v_ashrrev_i32_e32 v175, 31, v174
	v_lshlrev_b64 v[134:135], 13, v[174:175]
	v_lshl_add_u64 v[138:139], v[172:173], 0, v[134:135]
	global_load_dwordx4 v[142:145], v[138:139], off offset:16
	global_load_dwordx4 v[146:149], v[138:139], off
	global_load_dwordx4 v[134:137], v[138:139], off offset:528
	s_nop 0
	global_load_dwordx4 v[138:141], v[138:139], off offset:512
	v_and_b32_e32 v164, 64, v186
	v_xor_b32_e32 v155, 16, v186
	v_cmp_gt_u32_e32 vcc, 16, v154
	v_add_u32_e32 v154, 64, v164
	v_xor_b32_e32 v165, 32, v186
	v_cmp_lt_i32_e64 s[0:1], v155, v154
	v_lshlrev_b64 v[176:177], 12, v[170:171]
	v_lshl_add_u64 v[176:177], s[12:13], 0, v[176:177]
	v_cndmask_b32_e64 v155, v186, v155, s[0:1]
	v_cmp_lt_i32_e64 s[0:1], v165, v154
	v_lshlrev_b32_e32 v188, 2, v155
	v_readlane_b32 s38, v254, 41
	v_cndmask_b32_e64 v154, v186, v165, s[0:1]
	v_lshlrev_b32_e32 v187, 2, v154
	v_readlane_b32 s39, v254, 42
	v_readlane_b32 s66, v254, 9
	v_readlane_b32 s67, v254, 10
	v_readlane_b32 s68, v254, 11
	v_readlane_b32 s69, v254, 12
	v_readlane_b32 s70, v254, 13
	v_readlane_b32 s71, v254, 14
	v_readlane_b32 s72, v254, 15
	v_readlane_b32 s73, v254, 16
	v_readlane_b32 s74, v254, 17
	v_readlane_b32 s75, v254, 18
	v_readlane_b32 s76, v254, 19
	v_readlane_b32 s77, v254, 20
	v_readlane_b32 s78, v254, 21
	v_readlane_b32 s79, v254, 22
	v_or_b32_e32 v216, 32, v170
	v_ashrrev_i32_e32 v217, 31, v216
	v_lshlrev_b64 v[214:215], 13, v[216:217]
	v_lshl_add_u64 v[214:215], v[172:173], 0, v[214:215]
	global_load_dwordx4 v[230:233], v[214:215], off
	global_load_dwordx4 v[234:237], v[214:215], off offset:16
	global_load_dwordx4 v[238:241], v[214:215], off offset:512
	global_load_dwordx4 v[242:245], v[214:215], off offset:528
	v_or_b32_e32 v216, 48, v170
	v_ashrrev_i32_e32 v217, 31, v216
	v_lshlrev_b64 v[214:215], 13, v[216:217]
	v_lshl_add_u64 v[218:219], v[172:173], 0, v[214:215]
	global_load_dwordx4 v[222:225], v[218:219], off offset:16
	global_load_dwordx4 v[226:229], v[218:219], off
	global_load_dwordx4 v[214:217], v[218:219], off offset:528
	s_nop 0
	global_load_dwordx4 v[218:221], v[218:219], off offset:512
	s_waitcnt vmcnt(8)
	v_pk_mul_f32 v[166:167], v[158:159], s[26:27] op_sel_hi:[1,0]
	v_pk_mul_f32 v[168:169], v[156:157], s[26:27] op_sel_hi:[1,0]
	v_pk_mul_f32 v[164:165], v[162:163], s[26:27] op_sel_hi:[1,0]
	v_pk_mul_f32 v[162:163], v[160:161], s[26:27] op_sel_hi:[1,0]
	v_pk_mul_f32 v[158:159], v[196:197], s[26:27] op_sel_hi:[1,0]
	v_pk_mul_f32 v[160:161], v[194:195], s[26:27] op_sel_hi:[1,0]
	v_pk_mul_f32 v[154:155], v[190:191], s[26:27] op_sel_hi:[1,0]
	v_pk_fma_f32 v[194:195], v[8:9], v[166:167], v[200:201]
	v_pk_fma_f32 v[196:197], v[6:7], v[168:169], v[198:199]
	v_pk_fma_f32 v[198:199], v[12:13], v[164:165], v[204:205]
	v_pk_fma_f32 v[200:201], v[10:11], v[162:163], v[202:203]
	v_pk_fma_f32 v[202:203], v[40:41], v[158:159], v[208:209]
	v_pk_fma_f32 v[204:205], v[38:39], v[160:161], v[206:207]
	v_pk_mul_f32 v[156:157], v[192:193], s[26:27] op_sel_hi:[1,0]
	v_pk_fma_f32 v[208:209], v[42:43], v[154:155], v[210:211]
	v_mul_f32_e32 v189, v197, v197
	v_mul_f32_e32 v210, v195, v195
	v_cvt_pk_bf16_f32 v190, v196, v197
	v_cvt_pk_bf16_f32 v191, v194, v195
	v_mul_f32_e32 v195, v205, v205
	v_mul_f32_e32 v197, v203, v203
	v_pk_fma_f32 v[206:207], v[44:45], v[156:157], v[212:213]
	v_mul_f32_e32 v211, v201, v201
	v_mul_f32_e32 v212, v199, v199
	v_cvt_pk_bf16_f32 v193, v198, v199
	v_mul_f32_e32 v199, v209, v209
	v_fmac_f32_e32 v189, v196, v196
	v_fmac_f32_e32 v210, v194, v194
	v_fmac_f32_e32 v195, v204, v204
	v_fmac_f32_e32 v197, v202, v202
	v_cvt_pk_bf16_f32 v192, v200, v201
	v_mul_f32_e32 v201, v207, v207
	v_fmac_f32_e32 v211, v200, v200
	v_fmac_f32_e32 v199, v208, v208
	v_add_f32_e32 v189, v189, v210
	v_add_f32_e32 v194, v195, v197
	v_fmac_f32_e32 v212, v198, v198
	v_fmac_f32_e32 v201, v206, v206
	v_add_f32_e32 v189, v189, v211
	v_add_f32_e32 v194, v194, v199
	v_add_f32_e32 v189, v212, v189
	v_add_f32_e32 v194, v201, v194
	v_add_f32_e32 v189, v189, v194
	ds_bpermute_b32 v196, v188, v189
	v_lshl_add_u64 v[194:195], v[4:5], 1, v[176:177]
	global_store_dwordx4 v[194:195], v[190:193], off
	s_waitcnt lgkmcnt(0)
	v_add_f32_e32 v176, v189, v196
	ds_bpermute_b32 v177, v187, v176
	v_cvt_pk_bf16_f32 v190, v204, v205
	v_cvt_pk_bf16_f32 v191, v202, v203
	v_cvt_pk_bf16_f32 v192, v208, v209
	v_cvt_pk_bf16_f32 v193, v206, v207
	global_store_dwordx4 v[194:195], v[190:193], off offset:256
	s_and_saveexec_b64 s[0:1], vcc
	s_cbranch_execz .LBB0_745
	s_waitcnt lgkmcnt(0)
	v_add_f32_e32 v189, v176, v177
	s_lshl_b32 s34, s62, 2
	v_lshlrev_b64 v[176:177], 7, v[170:171]
	s_ashr_i32 s35, s34, 31
	v_lshl_add_u64 v[176:177], s[10:11], 0, v[176:177]
	v_lshl_add_u64 v[176:177], s[34:35], 2, v[176:177]
	s_lshl_b32 s4, s45, 2
	v_lshl_add_u64 v[176:177], v[176:177], 0, s[4:5]
	global_store_dword v[176:177], v189, off

; __device__ __forceinline__ unsigned cvt_pk_bf16(float lo, float hi) { const f32x2 v = {lo, hi}; return __builtin_bit_cast(unsigned, __builtin_convertvector(v, bf16x2_t)); }
;     __device__ __forceinline__ void operator()(g8::Acc& acc, const g8::Unit& u, int wr, int wc, int fr, int fq) const {
;     ...
;         for (int am = 0; am < 4; ++am) {
;             const int ai = am >> 1, m0 = (am & 1) * 2;
;             f32x4 xv[2][2][2];
; #pragma unroll
;             for (int mm = 0; mm < 2; ++mm)
; #pragma unroll
;                 for (int bj = 0; bj < 2; ++bj) { const size_t off = (size_t)(row0 + ai * 128 + (m0 + mm) * 16) * DM + col0 + bj * 128; xv[mm][bj][0] = *(const f32x4*)(x + off); xv[mm][bj][1] = *(const f32x4*)(x + off + 4); }
; #pragma unroll
;             for (int mm = 0; mm < 2; ++mm) { const int m = m0 + mm; const int row = row0 + ai * 128 + m * 16; float ss = 0.f;
; #pragma unroll
;                 for (int bj = 0; bj < 2; ++bj) { const size_t off = (size_t)row * DM + col0 + bj * 128;
;                     const f32x4 o0 = xv[mm][bj][0] + gt[bj][0] * acc[ai][bj][m][0], o1 = xv[mm][bj][1] + gt[bj][1] * acc[ai][bj][m][1];
;                     ss += (o0[0] * o0[0] + o0[1] * o0[1]) + (o0[2] * o0[2] + o0[3] * o0[3]) + (o1[0] * o1[0] + o1[1] * o1[1]) + (o1[2] * o1[2] + o1[3] * o1[3]);
;                     u32x4 w; w.x = cvt_pk_bf16(o0[0], o0[1]); w.y = cvt_pk_bf16(o0[2], o0[3]); w.z = cvt_pk_bf16(o1[0], o1[1]); w.w = cvt_pk_bf16(o1[2], o1[3]);
;                     *(u32x4*)(X1 + off) = w; }
;                 ss += __shfl_xor(ss, 16); ss += __shfl_xor(ss, 32);
;                 if (fq == 0) rowss2[(size_t)row * 32 + u.pn * 4 + wc] = ss; }
.LBB0_747:
	s_or_b64 exec, exec, s[0:1]
	v_or_b32_e32 v176, 32, v170
	v_ashrrev_i32_e32 v177, 31, v176
	s_waitcnt lgkmcnt(0)
	v_or_b32_e32 v174, 48, v170
	v_ashrrev_i32_e32 v175, 31, v174
	v_add_u32_e32 v136, 0x80, v170
	v_ashrrev_i32_e32 v137, 31, v136
	v_lshlrev_b64 v[134:135], 13, v[136:137]
	v_lshl_add_u64 v[134:135], v[172:173], 0, v[134:135]
	global_load_dwordx4 v[190:193], v[134:135], off
	global_load_dwordx4 v[194:197], v[134:135], off offset:16
	global_load_dwordx4 v[198:201], v[134:135], off offset:512
	global_load_dwordx4 v[202:205], v[134:135], off offset:528
	v_add_u32_e32 v136, 0x90, v170
	v_ashrrev_i32_e32 v137, 31, v136
	v_lshlrev_b64 v[134:135], 13, v[136:137]
	v_lshl_add_u64 v[138:139], v[172:173], 0, v[134:135]
	global_load_dwordx4 v[142:145], v[138:139], off offset:16
	global_load_dwordx4 v[146:149], v[138:139], off
	global_load_dwordx4 v[134:137], v[138:139], off offset:528
	s_nop 0
	global_load_dwordx4 v[138:141], v[138:139], off offset:512
	v_lshlrev_b64 v[246:247], 12, v[176:177]
	s_waitcnt vmcnt(14)
	v_pk_fma_f32 v[248:249], v[24:25], v[166:167], v[232:233]
	v_pk_fma_f32 v[250:251], v[22:23], v[168:169], v[230:231]
	v_pk_fma_f32 v[236:237], v[28:29], v[164:165], v[236:237]
	v_pk_fma_f32 v[234:235], v[26:27], v[162:163], v[234:235]
	v_pk_fma_f32 v[240:241], v[56:57], v[158:159], v[240:241]
	v_pk_fma_f32 v[238:239], v[54:55], v[160:161], v[238:239]
	v_pk_fma_f32 v[242:243], v[58:59], v[154:155], v[242:243]
	v_mul_f32_e32 v171, v251, v251
	v_mul_f32_e32 v189, v249, v249
	v_mul_f32_e32 v252, v235, v235
	v_mul_f32_e32 v253, v237, v237
	v_cvt_pk_bf16_f32 v232, v234, v235
	v_cvt_pk_bf16_f32 v233, v236, v237
	v_mul_f32_e32 v235, v239, v239
	v_mul_f32_e32 v237, v241, v241
	v_pk_fma_f32 v[244:245], v[60:61], v[156:157], v[244:245]
	v_cvt_pk_bf16_f32 v231, v248, v249
	v_mul_f32_e32 v249, v243, v243
	v_fmac_f32_e32 v171, v250, v250
	v_fmac_f32_e32 v189, v248, v248
	v_fmac_f32_e32 v235, v238, v238
	v_fmac_f32_e32 v237, v240, v240
	v_cvt_pk_bf16_f32 v230, v250, v251
	v_mul_f32_e32 v251, v245, v245
	v_fmac_f32_e32 v252, v234, v234
	v_fmac_f32_e32 v249, v242, v242
	v_add_f32_e32 v171, v171, v189
	v_add_f32_e32 v189, v235, v237
	v_fmac_f32_e32 v253, v236, v236
	v_fmac_f32_e32 v251, v244, v244
	v_add_f32_e32 v171, v171, v252
	v_add_f32_e32 v189, v189, v249
	v_add_f32_e32 v171, v253, v171
	v_add_f32_e32 v189, v251, v189
	v_add_f32_e32 v171, v171, v189
	ds_bpermute_b32 v189, v188, v171
	v_lshl_add_u64 v[234:235], s[12:13], 0, v[246:247]
	v_lshl_add_u64 v[234:235], v[4:5], 1, v[234:235]
	global_store_dwordx4 v[234:235], v[230:233], off
	s_waitcnt lgkmcnt(0)
	v_add_f32_e32 v171, v171, v189
	ds_bpermute_b32 v189, v187, v171
	v_cvt_pk_bf16_f32 v230, v238, v239
	v_cvt_pk_bf16_f32 v231, v240, v241
	v_cvt_pk_bf16_f32 v232, v242, v243
	v_cvt_pk_bf16_f32 v233, v244, v245
	global_store_dwordx4 v[234:235], v[230:233], off offset:256
	s_and_saveexec_b64 s[0:1], vcc
	s_cbranch_execz .LBB0_749
	s_lshl_b32 s34, s62, 2
	v_lshlrev_b64 v[176:177], 7, v[176:177]
	s_ashr_i32 s35, s34, 31
	v_lshl_add_u64 v[176:177], s[10:11], 0, v[176:177]
	v_lshl_add_u64 v[176:177], s[34:35], 2, v[176:177]
	s_lshl_b32 s4, s45, 2
	s_waitcnt lgkmcnt(0)
	v_add_f32_e32 v171, v171, v189
	v_lshl_add_u64 v[176:177], v[176:177], 0, s[4:5]
	global_store_dword v[176:177], v171, off
.LBB0_749:
	s_or_b64 exec, exec, s[0:1]
	v_pk_fma_f32 v[228:229], v[32:33], v[166:167], v[228:229]
	v_pk_fma_f32 v[226:227], v[30:31], v[168:169], v[226:227]
	v_pk_fma_f32 v[230:231], v[36:37], v[164:165], v[224:225]
	v_pk_fma_f32 v[224:225], v[34:35], v[162:163], v[222:223]
	v_mul_f32_e32 v222, v227, v227
	v_mul_f32_e32 v223, v229, v229
	v_fmac_f32_e32 v222, v226, v226
	v_fmac_f32_e32 v223, v228, v228
	v_add_f32_e32 v222, v222, v223
	v_mul_f32_e32 v223, v225, v225
	v_fmac_f32_e32 v223, v224, v224
	v_add_f32_e32 v222, v222, v223
	v_mul_f32_e32 v223, v231, v231
	v_fmac_f32_e32 v223, v230, v230
	v_pk_fma_f32 v[220:221], v[64:65], v[158:159], v[220:221]
	v_pk_fma_f32 v[218:219], v[62:63], v[160:161], v[218:219]
	v_add_f32_e32 v171, v223, v222
	v_cvt_pk_bf16_f32 v223, v228, v229
	v_pk_fma_f32 v[228:229], v[66:67], v[154:155], v[214:215]
	v_mul_f32_e32 v214, v219, v219
	v_mul_f32_e32 v215, v221, v221
	v_fmac_f32_e32 v214, v218, v218
	v_fmac_f32_e32 v215, v220, v220
	v_add_f32_e32 v214, v214, v215
	v_mul_f32_e32 v215, v229, v229
	v_cvt_pk_bf16_f32 v222, v226, v227
	v_pk_fma_f32 v[226:227], v[68:69], v[156:157], v[216:217]
	v_fmac_f32_e32 v215, v228, v228
	v_add_f32_e32 v214, v214, v215
	v_mul_f32_e32 v215, v227, v227
	v_fmac_f32_e32 v215, v226, v226
	v_add_f32_e32 v214, v215, v214
	v_add_f32_e32 v217, v171, v214
	ds_bpermute_b32 v171, v188, v217
	v_lshlrev_b64 v[176:177], 12, v[174:175]
	v_lshl_add_u64 v[214:215], s[12:13], 0, v[176:177]
	v_lshl_add_u64 v[176:177], v[4:5], 1, v[214:215]
	v_cvt_pk_bf16_f32 v224, v224, v225
	s_waitcnt lgkmcnt(0)
	v_add_f32_e32 v214, v217, v171
	ds_bpermute_b32 v215, v187, v214
	v_cvt_pk_bf16_f32 v225, v230, v231
	v_cvt_pk_bf16_f32 v216, v218, v219
	v_cvt_pk_bf16_f32 v217, v220, v221
	v_cvt_pk_bf16_f32 v218, v228, v229
	v_cvt_pk_bf16_f32 v219, v226, v227
	global_store_dwordx4 v[176:177], v[222:225], off
	global_store_dwordx4 v[176:177], v[216:219], off offset:256
	s_and_saveexec_b64 s[0:1], vcc
	s_cbranch_execz .LBB0_751
	s_waitcnt lgkmcnt(0)
	v_add_f32_e32 v216, v214, v215
	s_lshl_b32 s34, s62, 2
	v_lshlrev_b64 v[214:215], 7, v[174:175]
	s_ashr_i32 s35, s34, 31
	v_lshl_add_u64 v[214:215], s[10:11], 0, v[214:215]
	v_lshl_add_u64 v[214:215], s[34:35], 2, v[214:215]
	s_lshl_b32 s4, s45, 2
	v_lshl_add_u64 v[214:215], v[214:215], 0, s[4:5]
	global_store_dword v[214:215], v216, off
; __device__ __forceinline__ unsigned cvt_pk_bf16(float lo, float hi) { const f32x2 v = {lo, hi}; return __builtin_bit_cast(unsigned, __builtin_convertvector(v, bf16x2_t)); }
;     __device__ __forceinline__ void operator()(g8::Acc& acc, const g8::Unit& u, int wr, int wc, int fr, int fq) const {
;     ...
;         for (int am = 0; am < 4; ++am) {
;             const int ai = am >> 1, m0 = (am & 1) * 2;
;             f32x4 xv[2][2][2];
; #pragma unroll
;             for (int mm = 0; mm < 2; ++mm)
; #pragma unroll
;                 for (int bj = 0; bj < 2; ++bj) { const size_t off = (size_t)(row0 + ai * 128 + (m0 + mm) * 16) * DM + col0 + bj * 128; xv[mm][bj][0] = *(const f32x4*)(x + off); xv[mm][bj][1] = *(const f32x4*)(x + off + 4); }
; #pragma unroll
;             for (int mm = 0; mm < 2; ++mm) { const int m = m0 + mm; const int row = row0 + ai * 128 + m * 16; float ss = 0.f;
; #pragma unroll
;                 for (int bj = 0; bj < 2; ++bj) { const size_t off = (size_t)row * DM + col0 + bj * 128;
;                     const f32x4 o0 = xv[mm][bj][0] + gt[bj][0] * acc[ai][bj][m][0], o1 = xv[mm][bj][1] + gt[bj][1] * acc[ai][bj][m][1];
;                     ss += (o0[0] * o0[0] + o0[1] * o0[1]) + (o0[2] * o0[2] + o0[3] * o0[3]) + (o1[0] * o1[0] + o1[1] * o1[1]) + (o1[2] * o1[2] + o1[3] * o1[3]);
;                     u32x4 w; w.x = cvt_pk_bf16(o0[0], o0[1]); w.y = cvt_pk_bf16(o0[2], o0[3]); w.z = cvt_pk_bf16(o1[0], o1[1]); w.w = cvt_pk_bf16(o1[2], o1[3]);
;                     *(u32x4*)(X1 + off) = w; }
;                 ss += __shfl_xor(ss, 16); ss += __shfl_xor(ss, 32);
;                 if (fq == 0) rowss2[(size_t)row * 32 + u.pn * 4 + wc] = ss; }
.LBB0_751:
	s_or_b64 exec, exec, s[0:1]
	v_add_u32_e32 v176, 0x80, v170
	v_ashrrev_i32_e32 v177, 31, v176
	s_waitcnt lgkmcnt(0)
	v_add_u32_e32 v174, 0x90, v170
	v_ashrrev_i32_e32 v175, 31, v174
	v_add_u32_e32 v216, 0xa0, v170
	v_ashrrev_i32_e32 v217, 31, v216
	v_lshlrev_b64 v[214:215], 13, v[216:217]
	v_lshl_add_u64 v[214:215], v[172:173], 0, v[214:215]
	global_load_dwordx4 v[230:233], v[214:215], off
	global_load_dwordx4 v[234:237], v[214:215], off offset:16
	global_load_dwordx4 v[238:241], v[214:215], off offset:512
	global_load_dwordx4 v[242:245], v[214:215], off offset:528
	v_add_u32_e32 v216, 0xb0, v170
	v_ashrrev_i32_e32 v217, 31, v216
	v_lshlrev_b64 v[214:215], 13, v[216:217]
	v_lshl_add_u64 v[218:219], v[172:173], 0, v[214:215]
	global_load_dwordx4 v[222:225], v[218:219], off offset:16
	global_load_dwordx4 v[226:229], v[218:219], off
	global_load_dwordx4 v[214:217], v[218:219], off offset:528
	s_nop 0
	global_load_dwordx4 v[218:221], v[218:219], off offset:512
	v_lshlrev_b64 v[206:207], 12, v[176:177]
	s_waitcnt vmcnt(14)
	v_pk_fma_f32 v[208:209], v[72:73], v[166:167], v[192:193]
	v_pk_fma_f32 v[210:211], v[70:71], v[168:169], v[190:191]
	v_pk_fma_f32 v[196:197], v[76:77], v[164:165], v[196:197]
	v_pk_fma_f32 v[194:195], v[74:75], v[162:163], v[194:195]
	v_pk_fma_f32 v[200:201], v[104:105], v[158:159], v[200:201]
	v_pk_fma_f32 v[198:199], v[102:103], v[160:161], v[198:199]
	v_pk_fma_f32 v[202:203], v[106:107], v[154:155], v[202:203]
	v_mul_f32_e32 v171, v211, v211
	v_mul_f32_e32 v189, v209, v209
	v_mul_f32_e32 v212, v195, v195
	v_mul_f32_e32 v213, v197, v197
	v_cvt_pk_bf16_f32 v192, v194, v195
	v_cvt_pk_bf16_f32 v193, v196, v197
	v_mul_f32_e32 v195, v199, v199
	v_mul_f32_e32 v197, v201, v201
	v_pk_fma_f32 v[204:205], v[108:109], v[156:157], v[204:205]
	v_cvt_pk_bf16_f32 v191, v208, v209
	v_mul_f32_e32 v209, v203, v203
	v_fmac_f32_e32 v171, v210, v210
	v_fmac_f32_e32 v189, v208, v208
	v_fmac_f32_e32 v195, v198, v198
	v_fmac_f32_e32 v197, v200, v200
	v_cvt_pk_bf16_f32 v190, v210, v211
	v_mul_f32_e32 v211, v205, v205
	v_fmac_f32_e32 v212, v194, v194
	v_fmac_f32_e32 v209, v202, v202
	v_add_f32_e32 v171, v171, v189
	v_add_f32_e32 v189, v195, v197
	v_fmac_f32_e32 v213, v196, v196
	v_fmac_f32_e32 v211, v204, v204
	v_add_f32_e32 v171, v171, v212
	v_add_f32_e32 v189, v189, v209
	v_add_f32_e32 v171, v213, v171
	v_add_f32_e32 v189, v211, v189
	v_add_f32_e32 v171, v171, v189
	ds_bpermute_b32 v189, v188, v171
	v_lshl_add_u64 v[194:195], s[12:13], 0, v[206:207]
	v_lshl_add_u64 v[194:195], v[4:5], 1, v[194:195]
	global_store_dwordx4 v[194:195], v[190:193], off
	s_waitcnt lgkmcnt(0)
	v_add_f32_e32 v171, v171, v189
	ds_bpermute_b32 v189, v187, v171
	v_cvt_pk_bf16_f32 v190, v198, v199
	v_cvt_pk_bf16_f32 v191, v200, v201
	v_cvt_pk_bf16_f32 v192, v202, v203
	v_cvt_pk_bf16_f32 v193, v204, v205
	global_store_dwordx4 v[194:195], v[190:193], off offset:256
	s_and_saveexec_b64 s[0:1], vcc
	s_cbranch_execz .LBB0_753
	s_lshl_b32 s34, s62, 2
	v_lshlrev_b64 v[176:177], 7, v[176:177]
	s_ashr_i32 s35, s34, 31
	v_lshl_add_u64 v[176:177], s[10:11], 0, v[176:177]
	v_lshl_add_u64 v[176:177], s[34:35], 2, v[176:177]
	s_lshl_b32 s4, s45, 2
	s_waitcnt lgkmcnt(0)
	v_add_f32_e32 v171, v171, v189
	v_lshl_add_u64 v[176:177], v[176:177], 0, s[4:5]
	global_store_dword v[176:177], v171, off
.LBB0_753:
	s_or_b64 exec, exec, s[0:1]
	v_pk_fma_f32 v[148:149], v[80:81], v[166:167], v[148:149]
	v_pk_fma_f32 v[146:147], v[78:79], v[168:169], v[146:147]
	v_pk_fma_f32 v[190:191], v[84:85], v[164:165], v[144:145]
	v_pk_fma_f32 v[144:145], v[82:83], v[162:163], v[142:143]
	v_mul_f32_e32 v142, v147, v147
	v_mul_f32_e32 v143, v149, v149
	v_fmac_f32_e32 v142, v146, v146
	v_fmac_f32_e32 v143, v148, v148
	v_add_f32_e32 v142, v142, v143
	v_mul_f32_e32 v143, v145, v145
	v_fmac_f32_e32 v143, v144, v144
	v_add_f32_e32 v142, v142, v143
	v_mul_f32_e32 v143, v191, v191
	v_fmac_f32_e32 v143, v190, v190
	v_pk_fma_f32 v[140:141], v[112:113], v[158:159], v[140:141]
	v_pk_fma_f32 v[138:139], v[110:111], v[160:161], v[138:139]
	v_add_f32_e32 v171, v143, v142
	v_cvt_pk_bf16_f32 v143, v148, v149
	v_pk_fma_f32 v[148:149], v[114:115], v[154:155], v[134:135]
	v_mul_f32_e32 v134, v139, v139
	v_mul_f32_e32 v135, v141, v141
	v_fmac_f32_e32 v134, v138, v138
	v_fmac_f32_e32 v135, v140, v140
	v_add_f32_e32 v134, v134, v135
	v_mul_f32_e32 v135, v149, v149
	v_cvt_pk_bf16_f32 v142, v146, v147
	v_pk_fma_f32 v[146:147], v[116:117], v[156:157], v[136:137]
	v_fmac_f32_e32 v135, v148, v148
	v_add_f32_e32 v134, v134, v135
	v_mul_f32_e32 v135, v147, v147
	v_fmac_f32_e32 v135, v146, v146
	v_add_f32_e32 v134, v135, v134
	v_add_f32_e32 v137, v171, v134
	ds_bpermute_b32 v171, v188, v137
	v_lshlrev_b64 v[176:177], 12, v[174:175]
	v_lshl_add_u64 v[134:135], s[12:13], 0, v[176:177]
	v_lshl_add_u64 v[176:177], v[4:5], 1, v[134:135]
	v_cvt_pk_bf16_f32 v144, v144, v145
	s_waitcnt lgkmcnt(0)
	v_add_f32_e32 v134, v137, v171
	ds_bpermute_b32 v135, v187, v134
	v_cvt_pk_bf16_f32 v145, v190, v191
	v_cvt_pk_bf16_f32 v136, v138, v139
	v_cvt_pk_bf16_f32 v137, v140, v141
	v_cvt_pk_bf16_f32 v138, v148, v149
	v_cvt_pk_bf16_f32 v139, v146, v147
	global_store_dwordx4 v[176:177], v[142:145], off
	global_store_dwordx4 v[176:177], v[136:139], off offset:256
	s_and_saveexec_b64 s[0:1], vcc
	s_cbranch_execz .LBB0_755
	s_waitcnt lgkmcnt(0)
	v_add_f32_e32 v136, v134, v135
	s_lshl_b32 s34, s62, 2
	v_lshlrev_b64 v[134:135], 7, v[174:175]
	s_ashr_i32 s35, s34, 31
	v_lshl_add_u64 v[134:135], s[10:11], 0, v[134:135]
	v_lshl_add_u64 v[134:135], s[34:35], 2, v[134:135]
	s_lshl_b32 s4, s45, 2
	v_lshl_add_u64 v[134:135], v[134:135], 0, s[4:5]
	global_store_dword v[134:135], v136, off
; __device__ __forceinline__ unsigned cvt_pk_bf16(float lo, float hi) { const f32x2 v = {lo, hi}; return __builtin_bit_cast(unsigned, __builtin_convertvector(v, bf16x2_t)); }
;     __device__ __forceinline__ void operator()(g8::Acc& acc, const g8::Unit& u, int wr, int wc, int fr, int fq) const {
;     ...
;         for (int am = 0; am < 4; ++am) {
;             const int ai = am >> 1, m0 = (am & 1) * 2;
;             f32x4 xv[2][2][2];
; #pragma unroll
;             for (int mm = 0; mm < 2; ++mm)
; #pragma unroll
;                 for (int bj = 0; bj < 2; ++bj) { const size_t off = (size_t)(row0 + ai * 128 + (m0 + mm) * 16) * DM + col0 + bj * 128; xv[mm][bj][0] = *(const f32x4*)(x + off); xv[mm][bj][1] = *(const f32x4*)(x + off + 4); }
; #pragma unroll
;             for (int mm = 0; mm < 2; ++mm) { const int m = m0 + mm; const int row = row0 + ai * 128 + m * 16; float ss = 0.f;
; #pragma unroll
;                 for (int bj = 0; bj < 2; ++bj) { const size_t off = (size_t)row * DM + col0 + bj * 128;
;                     const f32x4 o0 = xv[mm][bj][0] + gt[bj][0] * acc[ai][bj][m][0], o1 = xv[mm][bj][1] + gt[bj][1] * acc[ai][bj][m][1];
;                     ss += (o0[0] * o0[0] + o0[1] * o0[1]) + (o0[2] * o0[2] + o0[3] * o0[3]) + (o1[0] * o1[0] + o1[1] * o1[1]) + (o1[2] * o1[2] + o1[3] * o1[3]);
;                     u32x4 w; w.x = cvt_pk_bf16(o0[0], o0[1]); w.y = cvt_pk_bf16(o0[2], o0[3]); w.z = cvt_pk_bf16(o1[0], o1[1]); w.w = cvt_pk_bf16(o1[2], o1[3]);
;                     *(u32x4*)(X1 + off) = w; }
;                 ss += __shfl_xor(ss, 16); ss += __shfl_xor(ss, 32);
;                 if (fq == 0) rowss2[(size_t)row * 32 + u.pn * 4 + wc] = ss; }
.LBB0_755:
	s_or_b64 exec, exec, s[0:1]
	v_add_u32_e32 v174, 0xa0, v170
	v_ashrrev_i32_e32 v175, 31, v174
	s_waitcnt lgkmcnt(0)
	v_add_u32_e32 v170, 0xb0, v170
	v_ashrrev_i32_e32 v171, 31, v170
	v_lshlrev_b64 v[172:173], 12, v[174:175]
	v_lshl_add_u64 v[172:173], s[12:13], 0, v[172:173]
	s_waitcnt vmcnt(6)
	v_pk_fma_f32 v[176:177], v[88:89], v[166:167], v[232:233]
	v_pk_fma_f32 v[246:247], v[86:87], v[168:169], v[230:231]
	v_pk_fma_f32 v[234:235], v[90:91], v[162:163], v[234:235]
	v_pk_fma_f32 v[240:241], v[120:121], v[158:159], v[240:241]
	v_pk_fma_f32 v[238:239], v[118:119], v[160:161], v[238:239]
	v_pk_fma_f32 v[236:237], v[92:93], v[164:165], v[236:237]
	v_pk_fma_f32 v[242:243], v[122:123], v[154:155], v[242:243]
	v_mul_f32_e32 v189, v247, v247
	v_mul_f32_e32 v248, v177, v177
	v_mul_f32_e32 v249, v235, v235
	v_cvt_pk_bf16_f32 v231, v176, v177
	v_cvt_pk_bf16_f32 v232, v234, v235
	v_mul_f32_e32 v177, v239, v239
	v_mul_f32_e32 v235, v241, v241
	v_pk_fma_f32 v[244:245], v[124:125], v[156:157], v[244:245]
	v_mul_f32_e32 v250, v237, v237
	v_cvt_pk_bf16_f32 v233, v236, v237
	v_mul_f32_e32 v237, v243, v243
	v_fmac_f32_e32 v189, v246, v246
	v_fmac_f32_e32 v248, v176, v176
	v_fmac_f32_e32 v177, v238, v238
	v_fmac_f32_e32 v235, v240, v240
	v_cvt_pk_bf16_f32 v230, v246, v247
	v_mul_f32_e32 v247, v245, v245
	v_fmac_f32_e32 v249, v234, v234
	v_fmac_f32_e32 v237, v242, v242
	v_add_f32_e32 v176, v189, v248
	v_add_f32_e32 v177, v177, v235
	v_fmac_f32_e32 v250, v236, v236
	v_fmac_f32_e32 v247, v244, v244
	v_add_f32_e32 v176, v176, v249
	v_add_f32_e32 v177, v177, v237
	v_add_f32_e32 v176, v250, v176
	v_add_f32_e32 v177, v247, v177
	v_add_f32_e32 v189, v176, v177
	ds_bpermute_b32 v234, v188, v189
	v_lshl_add_u64 v[176:177], v[4:5], 1, v[172:173]
	global_store_dwordx4 v[176:177], v[230:233], off
	s_waitcnt lgkmcnt(0)
	v_add_f32_e32 v172, v189, v234
	ds_bpermute_b32 v173, v187, v172
	v_cvt_pk_bf16_f32 v230, v238, v239
	v_cvt_pk_bf16_f32 v231, v240, v241
	v_cvt_pk_bf16_f32 v232, v242, v243
	v_cvt_pk_bf16_f32 v233, v244, v245
	global_store_dwordx4 v[176:177], v[230:233], off offset:256
	s_and_saveexec_b64 s[0:1], vcc
	s_cbranch_execz .LBB0_757
	s_waitcnt lgkmcnt(0)
	v_add_f32_e32 v176, v172, v173
	s_lshl_b32 s34, s62, 2
	v_lshlrev_b64 v[172:173], 7, v[174:175]
	s_ashr_i32 s35, s34, 31
	v_lshl_add_u64 v[172:173], s[10:11], 0, v[172:173]
	v_lshl_add_u64 v[172:173], s[34:35], 2, v[172:173]
	s_lshl_b32 s4, s45, 2
	v_lshl_add_u64 v[172:173], v[172:173], 0, s[4:5]
	global_store_dword v[172:173], v176, off
.LBB0_757:
	s_or_b64 exec, exec, s[0:1]
	v_pk_fma_f32 v[228:229], v[96:97], v[166:167], v[228:229]
	v_pk_fma_f32 v[226:227], v[94:95], v[168:169], v[226:227]
	v_pk_fma_f32 v[164:165], v[100:101], v[164:165], v[224:225]
	v_pk_fma_f32 v[224:225], v[98:99], v[162:163], v[222:223]
	v_mul_f32_e32 v222, v227, v227
	v_mul_f32_e32 v223, v229, v229
	v_fmac_f32_e32 v222, v226, v226
	v_fmac_f32_e32 v223, v228, v228
	v_add_f32_e32 v222, v222, v223
	v_mul_f32_e32 v223, v225, v225
	v_fmac_f32_e32 v223, v224, v224
	v_add_f32_e32 v222, v222, v223
	v_mul_f32_e32 v223, v165, v165
	v_fmac_f32_e32 v223, v164, v164
	v_pk_fma_f32 v[220:221], v[128:129], v[158:159], v[220:221]
	v_pk_fma_f32 v[218:219], v[126:127], v[160:161], v[218:219]
	v_add_f32_e32 v162, v223, v222
	v_cvt_pk_bf16_f32 v222, v226, v227
	v_pk_fma_f32 v[226:227], v[132:133], v[156:157], v[216:217]
	v_pk_fma_f32 v[216:217], v[130:131], v[154:155], v[214:215]
	v_mul_f32_e32 v214, v219, v219
	v_mul_f32_e32 v215, v221, v221
	v_fmac_f32_e32 v214, v218, v218
	v_fmac_f32_e32 v215, v220, v220
	v_add_f32_e32 v214, v214, v215
	v_mul_f32_e32 v215, v217, v217
	v_fmac_f32_e32 v215, v216, v216
	v_add_f32_e32 v214, v214, v215
	v_mul_f32_e32 v215, v227, v227
	v_fmac_f32_e32 v215, v226, v226
	v_add_f32_e32 v214, v215, v214
	v_add_f32_e32 v154, v162, v214
	ds_bpermute_b32 v155, v188, v154
	s_waitcnt lgkmcnt(1)
	v_lshlrev_b64 v[172:173], 12, v[170:171]
	v_lshl_add_u64 v[214:215], s[12:13], 0, v[172:173]
	v_cvt_pk_bf16_f32 v223, v228, v229
	v_lshl_add_u64 v[228:229], v[4:5], 1, v[214:215]
	s_waitcnt lgkmcnt(0)
	v_add_f32_e32 v4, v154, v155
	ds_bpermute_b32 v5, v187, v4
	v_cvt_pk_bf16_f32 v224, v224, v225
	v_cvt_pk_bf16_f32 v225, v164, v165
	v_cvt_pk_bf16_f32 v214, v218, v219
	v_cvt_pk_bf16_f32 v215, v220, v221
	v_cvt_pk_bf16_f32 v216, v216, v217
	v_cvt_pk_bf16_f32 v217, v226, v227
	global_store_dwordx4 v[228:229], v[222:225], off
	global_store_dwordx4 v[228:229], v[214:217], off offset:256
	s_and_saveexec_b64 s[0:1], vcc
	s_cbranch_execz .LBB0_759
	s_waitcnt lgkmcnt(0)
	v_add_f32_e32 v214, v4, v5
	s_lshl_b32 s34, s62, 2
	v_lshlrev_b64 v[4:5], 7, v[170:171]
	s_ashr_i32 s35, s34, 31
	v_lshl_add_u64 v[4:5], s[10:11], 0, v[4:5]
	v_lshl_add_u64 v[4:5], s[34:35], 2, v[4:5]
	s_lshl_b32 s4, s45, 2
	v_lshl_add_u64 v[4:5], v[4:5], 0, s[4:5]
	global_store_dword v[4:5], v214, off

; __device__ __forceinline__ void p6_route(const Params& P, LAS unsigned char* lds, int tid, int blk, int G) {
;     ...
;         for (int k = tid; k < 2048; k += NTHREADS) { gm[k] = P.in[18][k] * (1.0f + mod[(size_t)b * NMOD + 4 * DM + k]); sh[k] = mod[(size_t)b * NMOD + 3 * DM + k]; }
;         if (tid < 32) lcnt[tid] = 0;
;         if (tid >= 64 && tid < 128) { const int r = tid - 64; float tot2 = 0.f; const f32x4* pp = (const f32x4*)(rowss2 + (size_t)(rb * 64 + r) * 32);
; #pragma unroll
;             for (int i = 0; i < 8; ++i) { const f32x4 v = pp[i]; tot2 += (v[0] + v[1]) + (v[2] + v[3]); }
;             r2s[r] = rsqrtf(tot2 * (1.0f / 2048.0f) + 1e-6f); }
.LBB0_827:
	global_load_dword v12, v[4:5], off
	global_load_dword v13, v[2:3], off
	v_add_co_u32_e32 v8, vcc, 0xffffe000, v2
	s_nop 1
	v_addc_co_u32_e32 v9, vcc, -1, v3, vcc
	global_load_dword v14, v[8:9], off
	v_lshl_add_u64 v[4:5], v[4:5], 0, s[34:35]
	v_lshl_add_u64 v[2:3], v[2:3], 0, s[34:35]
	global_load_dword v15, v[4:5], off
	global_load_dword v16, v[2:3], off
	v_add_co_u32_e32 v8, vcc, 0xffffe000, v2
	s_nop 1
	v_addc_co_u32_e32 v9, vcc, -1, v3, vcc
	global_load_dword v17, v[8:9], off
	v_lshl_add_u64 v[4:5], v[4:5], 0, s[34:35]
	v_lshl_add_u64 v[2:3], v[2:3], 0, s[34:35]
	global_load_dword v18, v[4:5], off
	global_load_dword v19, v[2:3], off
	v_add_co_u32_e32 v8, vcc, 0xffffe000, v2
	s_nop 1
	v_addc_co_u32_e32 v9, vcc, -1, v3, vcc
	global_load_dword v20, v[8:9], off
	v_lshl_add_u64 v[4:5], v[4:5], 0, s[34:35]
	v_lshl_add_u64 v[2:3], v[2:3], 0, s[34:35]
	global_load_dword v21, v[4:5], off
	global_load_dword v22, v[2:3], off
	v_add_co_u32_e32 v8, vcc, 0xffffe000, v2
	s_nop 1
	v_addc_co_u32_e32 v9, vcc, -1, v3, vcc
	global_load_dword v23, v[8:9], off
	s_waitcnt vmcnt(0)
	v_add_f32_e32 v9, 1.0, v13
	v_mul_f32_e32 v9, v12, v9
	ds_write2st64_b32 v6, v9, v14 offset1:32
	v_add_u32_e32 v6, 0x800, v6
	v_add_f32_e32 v9, 1.0, v16
	v_mul_f32_e32 v9, v15, v9
	ds_write2st64_b32 v6, v9, v17 offset1:32
	v_add_u32_e32 v6, 0x800, v6
	v_add_f32_e32 v9, 1.0, v19
	v_mul_f32_e32 v9, v18, v9
	ds_write2st64_b32 v6, v9, v20 offset1:32
	v_add_u32_e32 v6, 0x800, v6
	v_add_f32_e32 v9, 1.0, v22
	v_mul_f32_e32 v9, v21, v9
	ds_write2st64_b32 v6, v9, v23 offset1:32
	s_or_b64 exec, exec, s[0:1]
	s_and_saveexec_b64 s[0:1], s[6:7]
	ds_write_b32 v226, v179
	s_or_b64 exec, exec, s[0:1]
	s_and_saveexec_b64 s[0:1], s[8:9]
	s_cbranch_execz .LBB0_832
	v_or_b32_e32 v2, s57, v227
	v_ashrrev_i32_e32 v3, 31, v2
	v_lshlrev_b64 v[2:3], 7, v[2:3]
	v_lshl_add_u64 v[30:31], s[4:5], 0, v[2:3]
	global_load_dwordx4 v[2:5], v[30:31], off
	global_load_dwordx4 v[6:9], v[30:31], off offset:16
	global_load_dwordx4 v[10:13], v[30:31], off offset:32
	global_load_dwordx4 v[14:17], v[30:31], off offset:48
	global_load_dwordx4 v[18:21], v[30:31], off offset:64
	global_load_dwordx4 v[22:25], v[30:31], off offset:80
	global_load_dwordx4 v[26:29], v[30:31], off offset:96
	s_nop 0
	global_load_dwordx4 v[30:33], v[30:31], off offset:112
	s_waitcnt vmcnt(7)
	v_mov_b32_e32 v34, v2
	s_waitcnt vmcnt(6)
	v_mov_b32_e32 v35, v6
	v_mov_b32_e32 v6, v3
	v_mov_b32_e32 v2, v4
	v_mov_b32_e32 v3, v8
	v_mov_b32_e32 v8, v5
	s_waitcnt vmcnt(5)
	v_mov_b32_e32 v4, v11
	v_mov_b32_e32 v5, v12
	v_mov_b32_e32 v11, v13
	v_pk_add_f32 v[6:7], v[34:35], v[6:7]
	v_pk_add_f32 v[2:3], v[2:3], v[8:9]
	v_pk_add_f32 v[4:5], v[4:5], v[10:11]
	v_pk_add_f32 v[2:3], v[6:7], v[2:3]
	v_pk_add_f32 v[4:5], v[4:5], v[4:5] op_sel:[0,1] op_sel_hi:[1,0]
	v_add_f32_e32 v2, 0, v2
	s_waitcnt vmcnt(4)
	v_add_f32_e32 v12, v14, v15
	v_add_f32_e32 v14, v16, v17
	s_waitcnt vmcnt(3)
	v_mov_b32_e32 v17, v18
	v_mov_b32_e32 v13, v20
	v_mov_b32_e32 v15, v21
	v_mov_b32_e32 v5, v19
	v_add_f32_e32 v16, v2, v3
	s_waitcnt vmcnt(2)
	v_mov_b32_e32 v20, v23
	v_mov_b32_e32 v21, v24
	v_mov_b32_e32 v23, v25
	v_pk_add_f32 v[8:9], v[12:13], v[14:15]
	v_pk_add_f32 v[2:3], v[16:17], v[4:5]
	v_pk_add_f32 v[10:11], v[20:21], v[22:23]
	v_pk_add_f32 v[2:3], v[2:3], v[8:9]
	v_pk_add_f32 v[6:7], v[10:11], v[10:11] op_sel:[0,1] op_sel_hi:[1,0]
	v_pk_add_f32 v[2:3], v[2:3], v[2:3] op_sel:[0,1] op_sel_hi:[1,0]
	s_waitcnt vmcnt(1)
	v_add_f32_e32 v24, v26, v27
	v_add_f32_e32 v26, v28, v29
	s_waitcnt vmcnt(0)
	v_mov_b32_e32 v25, v32
	v_mov_b32_e32 v27, v33
	v_mov_b32_e32 v7, v31
	v_mov_b32_e32 v3, v30
	v_pk_add_f32 v[12:13], v[24:25], v[26:27]
	v_pk_add_f32 v[2:3], v[2:3], v[6:7]
	s_nop 0
	v_pk_add_f32 v[2:3], v[2:3], v[12:13]
	s_nop 0
	v_add_f32_e32 v2, v2, v3
	v_fmamk_f32 v2, v2, 0x3a000000, v236
	v_mul_f32_e32 v3, 0x4b800000, v2
	v_cmp_gt_f32_e32 vcc, s46, v2
	s_nop 1
	v_cndmask_b32_e32 v2, v2, v3, vcc
	v_rsq_f32_e32 v2, v2
	s_nop 0
	v_mul_f32_e32 v3, 0x45800000, v2
	v_cndmask_b32_e32 v2, v2, v3, vcc
	ds_write_b32 v228, v2
